# attention: row-sum reduction interleaved into the issue gaps of the last four PV MFMAs (temporaries renamed to free registers), same operations
# baseline (speedup 1.0000x reference)
; #define AT_TRR(dst, off) asm volatile("ds_read_b64_tr_b16 %0, %1 offset:%c2" : "=&v"(dst) : "v"(vaddr), "i"(off) : "memory")
; #define AT_PIN() do { _Pragma("unroll") for (int g_ = 0; g_ < 4; ++g_) { __builtin_amdgcn_sched_group_barrier(0x008, 1, 0); __builtin_amdgcn_sched_group_barrier(0x400, 2, 0); __builtin_amdgcn_sched_group_barrier(0x002, 2, 0); } \
;                 __builtin_amdgcn_sched_barrier(0); } while (0)
; __device__ __forceinline__ void attn_unit(const Frame& F, const bf16* __restrict__ proj, bf16* mix, const float* relb, const float* subg, int h, int qb, float lam, float one_m_li) {
;     ...
;             AT_EXPBLK(0);
;             const unsigned vaddr = (unsigned)(uintptr_t)(lds + cur * STAGE + 16384 + (4 * hi + ((lane & 15) >> 2)) * 64 + ((lane >> 4) & 1) * 32 + (lane & 3) * 8);
;             s16x4 fl[2][4], fh[2][4];
;     ...
; #pragma unroll
;             for (int eb = 0; eb < 4; ++eb) { AT_TRR(fl[0][eb], eb * 4096); AT_TRR(fh[0][eb], eb * 4096 + 512); }
;     ...
;             AT_PVSTEP(0); AT_EXPBLK(1); AT_PIN();
;             AT_PVSTEP(1); AT_EXPBLK(2); AT_PIN();
;             AT_PVSTEP(2); AT_EXPBLK(3); AT_PIN();
;             AT_PVSTEP(3); __builtin_amdgcn_sched_barrier(0);
;             lsum += (lpart[0] + lpart[1]) + (lpart[2] + lpart[3]);
.LBB0_579:
	v_exp_f32_e32 v169, v96
	v_add_u32_e32 v96, s79, v218
	v_add3_u32 v96, v96, v219, v220
	v_exp_f32_e32 v177, v99
	v_exp_f32_e32 v99, v102
	v_add3_u32 v102, v96, v221, s17
	ds_read_b64_tr_b16 v[182:183], v102 offset:0
	ds_read_b64_tr_b16 v[184:185], v102 offset:512
	ds_read_b64_tr_b16 v[236:237], v102 offset:4096
	ds_read_b64_tr_b16 v[238:239], v102 offset:4608
	ds_read_b64_tr_b16 v[240:241], v102 offset:8192
	ds_read_b64_tr_b16 v[242:243], v102 offset:8704
	ds_read_b64_tr_b16 v[244:245], v102 offset:12288
	ds_read_b64_tr_b16 v[246:247], v102 offset:12800
	ds_read_b64_tr_b16 v[248:249], v102 offset:1024
	ds_read_b64_tr_b16 v[250:251], v102 offset:1536
	ds_read_b64_tr_b16 v[228:229], v102 offset:5120
	ds_read_b64_tr_b16 v[230:231], v102 offset:5632
	ds_read_b64_tr_b16 v[196:197], v102 offset:9216
	ds_read_b64_tr_b16 v[198:199], v102 offset:9728
	ds_read_b64_tr_b16 v[200:201], v102 offset:13312
	v_exp_f32_e32 v97, v97
	v_exp_f32_e32 v175, v98
	v_exp_f32_e32 v171, v100
	v_exp_f32_e32 v173, v101
	v_exp_f32_e32 v101, v103
	ds_read_b64_tr_b16 v[202:203], v102 offset:13824
	s_waitcnt lgkmcnt(8)
	v_cvt_pk_bf16_f32 v178, v169, v97
	v_cvt_pk_bf16_f32 v179, v175, v177
	v_cvt_pk_bf16_f32 v180, v171, v173
	v_cvt_pk_bf16_f32 v181, v99, v101
	s_nop 1
	v_mfma_f32_32x32x16_bf16 v[48:63], v[182:185], v[178:181], v[48:63]
	v_exp_f32_e32 v103, v104
	v_exp_f32_e32 v105, v105
	v_mfma_f32_32x32x16_bf16 v[32:47], v[236:239], v[178:181], v[32:47]
	v_exp_f32_e32 v183, v106
	v_exp_f32_e32 v185, v107
	v_cvt_pk_bf16_f32 v236, v103, v105
	v_cvt_pk_bf16_f32 v237, v183, v185
	v_mfma_f32_32x32x16_bf16 v[16:31], v[240:243], v[178:181], v[16:31]
	v_exp_f32_e32 v107, v110
	v_mfma_f32_32x32x16_bf16 v[0:15], v[244:247], v[178:181], v[0:15]
	v_exp_f32_e32 v181, v109
	v_exp_f32_e32 v109, v111
	v_exp_f32_e32 v179, v108
	v_cvt_pk_bf16_f32 v239, v107, v109
	v_cvt_pk_bf16_f32 v238, v179, v181
	ds_read_b64_tr_b16 v[240:241], v102 offset:2048
	ds_read_b64_tr_b16 v[242:243], v102 offset:2560
	ds_read_b64_tr_b16 v[244:245], v102 offset:6144
	ds_read_b64_tr_b16 v[246:247], v102 offset:6656
	ds_read_b64_tr_b16 v[232:233], v102 offset:10240
	ds_read_b64_tr_b16 v[234:235], v102 offset:10752
	ds_read_b64_tr_b16 v[224:225], v102 offset:14336
	ds_read_b64_tr_b16 v[226:227], v102 offset:14848
	s_waitcnt lgkmcnt(8)
	s_nop 1
	v_mfma_f32_32x32x16_bf16 v[48:63], v[248:251], v[236:239], v[48:63]
	v_exp_f32_e32 v168, v80
	v_exp_f32_e32 v96, v81
	s_nop 0
	v_cvt_pk_bf16_f32 v80, v168, v96
	v_mfma_f32_32x32x16_bf16 v[32:47], v[228:231], v[236:239], v[32:47]
	v_exp_f32_e32 v174, v82
	v_exp_f32_e32 v176, v83
	s_nop 0
	v_cvt_pk_bf16_f32 v81, v174, v176
	v_mfma_f32_32x32x16_bf16 v[16:31], v[196:199], v[236:239], v[16:31]
	v_exp_f32_e32 v170, v84
	v_exp_f32_e32 v172, v85
	s_nop 0
	v_cvt_pk_bf16_f32 v82, v170, v172
	v_mfma_f32_32x32x16_bf16 v[0:15], v[200:203], v[236:239], v[0:15]
	v_exp_f32_e32 v98, v86
	v_exp_f32_e32 v100, v87
	s_nop 0
	v_cvt_pk_bf16_f32 v83, v98, v100
	ds_read_b64_tr_b16 v[84:85], v102 offset:3072
	ds_read_b64_tr_b16 v[86:87], v102 offset:3584
	ds_read_b64_tr_b16 v[196:197], v102 offset:7168
	ds_read_b64_tr_b16 v[198:199], v102 offset:7680
	ds_read_b64_tr_b16 v[200:201], v102 offset:11264
	ds_read_b64_tr_b16 v[202:203], v102 offset:11776
	ds_read_b64_tr_b16 v[228:229], v102 offset:15360
	ds_read_b64_tr_b16 v[230:231], v102 offset:15872
	s_waitcnt lgkmcnt(8)
	s_nop 1
	v_mfma_f32_32x32x16_bf16 v[48:63], v[240:243], v[80:83], v[48:63]
	v_exp_f32_e32 v102, v88
	v_exp_f32_e32 v104, v89
	s_nop 0
	v_cvt_pk_bf16_f32 v88, v102, v104
	v_mfma_f32_32x32x16_bf16 v[32:47], v[244:247], v[80:83], v[32:47]
	v_exp_f32_e32 v182, v90
	v_exp_f32_e32 v184, v91
	s_nop 0
	v_cvt_pk_bf16_f32 v89, v182, v184
	v_mfma_f32_32x32x16_bf16 v[16:31], v[232:235], v[80:83], v[16:31]
	v_exp_f32_e32 v178, v92
	v_exp_f32_e32 v180, v93
	s_nop 0
	v_cvt_pk_bf16_f32 v90, v178, v180
	v_mfma_f32_32x32x16_bf16 v[0:15], v[224:227], v[80:83], v[0:15]
	v_exp_f32_e32 v106, v94
	v_exp_f32_e32 v108, v95
	s_nop 0
	v_cvt_pk_bf16_f32 v91, v106, v108
	s_waitcnt lgkmcnt(0)
	s_nop 1
	v_mfma_f32_32x32x16_bf16 v[48:63], v[84:87], v[88:91], v[48:63]
	v_add_f32_e64 v82, v170, v172
	v_add_f32_e64 v83, v171, v173
	v_add_f32_e64 v132, v98, v100
	v_add_f32_e64 v133, v99, v101
	v_add_f32_e64 v80, v174, v176
	v_mfma_f32_32x32x16_bf16 v[32:47], v[196:199], v[88:91], v[32:47]
	v_add_f32_e64 v81, v175, v177
	v_pk_add_f32 v[134:135], v[106:107], v[108:109]
	v_pk_add_f32 v[82:83], v[82:83], v[132:133]
	v_pk_add_f32 v[132:133], v[168:169], v[96:97]
	v_mfma_f32_32x32x16_bf16 v[16:31], v[200:203], v[88:91], v[16:31]
	v_pk_add_f32 v[80:81], v[132:133], v[80:81]
	v_pk_add_f32 v[132:133], v[178:179], v[180:181]
	v_pk_add_f32 v[80:81], v[80:81], v[82:83]
	v_pk_add_f32 v[82:83], v[182:183], v[184:185]
	v_mfma_f32_32x32x16_bf16 v[0:15], v[228:231], v[88:91], v[0:15]
	v_pk_add_f32 v[132:133], v[132:133], v[134:135]
	v_pk_add_f32 v[134:135], v[102:103], v[104:105]
	s_nop 0
	v_pk_add_f32 v[82:83], v[134:135], v[82:83]
	s_nop 0
	v_pk_add_f32 v[82:83], v[82:83], v[132:133]
	s_nop 0
	v_pk_add_f32 v[80:81], v[80:81], v[82:83]
	s_nop 0
	v_add_f32_e32 v80, v80, v81
	v_add_f32_e32 v163, v163, v80
